# attention v4 schedule with the tile K fragment LDS reads issued before the next-tile global loads
# speedup vs baseline: 1.0032x; 1.0032x over previous
.Lfa_loop:
.Lfa_body_0:
	ds_read_b128 v[114:117], v130 offset:64
	ds_read_b128 v[118:121], v130 offset:96
	ds_read_b128 v[122:125], v130 offset:128
	ds_read_b128 v[132:135], v130 offset:160
	ds_read_b128 v[136:139], v130 offset:192
	ds_read_b128 v[140:143], v130 offset:224
	ds_read_b128 v[146:149], v130 offset:6720
	ds_read_b128 v[150:153], v130 offset:6752
	s_add_i32 s31, s30, 1
	s_cmp_lt_u32 s31, s65
	s_cbranch_scc0 .Lfa_noload_0
	global_load_dwordx4 v[98:101], v[112:113], off
	global_load_dwordx4 v[94:97], v[110:111], off
	s_cmp_lg_u32 s43, 0
	s_cbranch_scc0 .Lfa_noload_0
	global_load_dwordx4 v[90:93], v[108:109], off
.Lfa_noload_0:
	s_waitcnt lgkmcnt(7)
	v_mfma_f32_32x32x16_bf16 v[34:49], v[114:117], v[86:89], 0
	v_add_f32_e32 v105, v105, v50
	v_add_f32_e32 v145, v145, v51
	v_add_f32_e32 v105, v105, v52
	ds_read_b128 v[154:157], v130 offset:6784
	s_waitcnt lgkmcnt(7)
	v_mfma_f32_32x32x16_bf16 v[34:49], v[118:121], v[82:85], v[34:49]
	v_add_f32_e32 v145, v145, v53
	v_add_f32_e32 v105, v105, v54
	v_add_f32_e32 v145, v145, v55
	ds_read_b128 v[158:161], v130 offset:6816
	s_waitcnt lgkmcnt(7)
	v_mfma_f32_32x32x16_bf16 v[34:49], v[122:125], v[78:81], v[34:49]
	v_add_f32_e32 v105, v105, v56
	v_add_f32_e32 v145, v145, v57
	v_add_f32_e32 v105, v105, v58
	ds_read_b128 v[162:165], v130 offset:6848
	s_waitcnt lgkmcnt(7)
	v_mfma_f32_32x32x16_bf16 v[34:49], v[132:135], v[74:77], v[34:49]
	v_add_f32_e32 v145, v145, v59
	v_add_f32_e32 v105, v105, v60
	v_add_f32_e32 v145, v145, v61
	ds_read_b128 v[166:169], v130 offset:6880
	s_waitcnt lgkmcnt(7)
	v_mfma_f32_32x32x16_bf16 v[34:49], v[136:139], v[70:73], v[34:49]
	v_add_f32_e32 v105, v105, v62
	v_add_f32_e32 v145, v145, v63
	s_waitcnt lgkmcnt(6)
	v_mfma_f32_32x32x16_bf16 v[34:49], v[140:143], v[66:69], v[34:49]
	v_add_f32_e32 v105, v105, v64
	v_add_f32_e32 v145, v145, v65
	s_waitcnt lgkmcnt(5)
	v_mfma_f32_32x32x16_bf16 v[50:65], v[146:149], v[86:89], 0
	ds_read_b128 v[114:117], v107 offset:13376
	ds_read_b128 v[118:121], v107 offset:17984
	ds_read_b128 v[122:125], v107 offset:13408
	ds_read_b128 v[132:135], v107 offset:18016
	ds_read_b128 v[136:139], v107 offset:13440
	ds_read_b128 v[140:143], v107 offset:18048
	ds_read_b128 v[146:149], v107 offset:13472
	s_waitcnt lgkmcnt(11)
	v_mfma_f32_32x32x16_bf16 v[50:65], v[150:153], v[82:85], v[50:65]
	ds_read_b128 v[150:153], v107 offset:18080
	v_lshl_add_u64 v[112:113], v[112:113], 0, s[12:13]
	v_lshl_add_u64 v[110:111], v[110:111], 0, v[194:195]
	v_lshl_add_u64 v[108:109], v[108:109], 0, s[10:11]
	v_exp_f32_e32 v34, v34
	v_exp_f32_e32 v35, v35
	s_waitcnt lgkmcnt(11)
	v_mfma_f32_32x32x16_bf16 v[50:65], v[154:157], v[78:81], v[50:65]
	v_exp_f32_e32 v36, v36
	v_exp_f32_e32 v37, v37
	v_exp_f32_e32 v38, v38
	s_waitcnt lgkmcnt(10)
	v_mfma_f32_32x32x16_bf16 v[50:65], v[158:161], v[74:77], v[50:65]
	v_exp_f32_e32 v39, v39
	v_exp_f32_e32 v40, v40
	v_exp_f32_e32 v41, v41
	v_cvt_pk_bf16_f32 v154, v34, v35
	s_waitcnt lgkmcnt(9)
	v_mfma_f32_32x32x16_bf16 v[50:65], v[162:165], v[70:73], v[50:65]
	v_cvt_pk_bf16_f32 v155, v36, v37
	v_cvt_pk_bf16_f32 v156, v38, v39
	v_exp_f32_e32 v42, v42
	v_exp_f32_e32 v43, v43
	s_waitcnt lgkmcnt(8)
	v_mfma_f32_32x32x16_bf16 v[50:65], v[166:169], v[66:69], v[50:65]
	v_cvt_pk_bf16_f32 v157, v40, v41
	v_exp_f32_e32 v44, v44
	v_exp_f32_e32 v45, v45
	v_exp_f32_e32 v46, v46
	s_waitcnt lgkmcnt(7)
	v_mfma_f32_32x32x16_bf16 v[18:33], v[114:117], v[154:157], v[18:33]
	v_exp_f32_e32 v47, v47
	v_exp_f32_e32 v48, v48
	v_exp_f32_e32 v49, v49
	v_cvt_pk_bf16_f32 v158, v42, v43
	s_waitcnt lgkmcnt(6)
	v_mfma_f32_32x32x16_bf16 v[2:17], v[118:121], v[154:157], v[2:17]
	v_cvt_pk_bf16_f32 v159, v44, v45
	v_cvt_pk_bf16_f32 v160, v46, v47
	v_cvt_pk_bf16_f32 v161, v48, v49
	v_add_f32_e32 v105, v105, v34
	v_add_f32_e32 v145, v145, v35
	v_add_f32_e32 v105, v105, v36
	v_exp_f32_e32 v50, v50
	s_waitcnt lgkmcnt(5)
	v_mfma_f32_32x32x16_bf16 v[18:33], v[122:125], v[158:161], v[18:33]
	v_exp_f32_e32 v51, v51
	v_exp_f32_e32 v52, v52
	v_exp_f32_e32 v53, v53
	s_waitcnt lgkmcnt(4)
	v_mfma_f32_32x32x16_bf16 v[2:17], v[132:135], v[158:161], v[2:17]
	v_exp_f32_e32 v54, v54
	v_exp_f32_e32 v55, v55
	v_exp_f32_e32 v56, v56
	v_exp_f32_e32 v57, v57
	v_cvt_pk_bf16_f32 v162, v50, v51
	v_cvt_pk_bf16_f32 v163, v52, v53
	v_cvt_pk_bf16_f32 v164, v54, v55
	v_cvt_pk_bf16_f32 v165, v56, v57
	v_add_f32_e32 v145, v145, v37
	v_add_f32_e32 v105, v105, v38
	s_waitcnt lgkmcnt(3)
	v_mfma_f32_32x32x16_bf16 v[18:33], v[136:139], v[162:165], v[18:33]
	v_exp_f32_e32 v58, v58
	v_exp_f32_e32 v59, v59
	v_exp_f32_e32 v60, v60
	s_waitcnt lgkmcnt(2)
	v_mfma_f32_32x32x16_bf16 v[2:17], v[140:143], v[162:165], v[2:17]
	v_exp_f32_e32 v61, v61
	v_exp_f32_e32 v62, v62
	v_exp_f32_e32 v63, v63
	v_exp_f32_e32 v64, v64
	v_exp_f32_e32 v65, v65
	v_cvt_pk_bf16_f32 v166, v58, v59
	v_cvt_pk_bf16_f32 v167, v60, v61
	v_cvt_pk_bf16_f32 v168, v62, v63
	v_cvt_pk_bf16_f32 v169, v64, v65
	v_add_f32_e32 v145, v145, v39
	v_add_f32_e32 v105, v105, v40
	s_waitcnt lgkmcnt(1)
	v_mfma_f32_32x32x16_bf16 v[18:33], v[146:149], v[166:169], v[18:33]
	v_add_f32_e32 v145, v145, v41
	v_add_f32_e32 v105, v105, v42
	v_add_f32_e32 v145, v145, v43
	v_add_f32_e32 v105, v105, v44
	v_add_f32_e32 v145, v145, v45
	s_waitcnt lgkmcnt(0)
	v_mfma_f32_32x32x16_bf16 v[2:17], v[150:153], v[166:169], v[2:17]
	v_add_f32_e32 v105, v105, v46
	v_add_f32_e32 v145, v145, v47
	v_add_f32_e32 v105, v105, v48
	v_add_f32_e32 v145, v145, v49
	s_cmp_lt_u32 s31, s65
	s_cbranch_scc0 .Lfa_nowrite_0
	s_waitcnt vmcnt(0)
	ds_write_b128 v106, v[98:101] offset:22592
	ds_write_b128 v128, v[94:97] offset:22592
	s_cmp_lg_u32 s43, 0
	s_cbranch_scc0 .Lfa_nowrite_0
	ds_write_b128 v129, v[90:93] offset:35904

.Lfa_body_1:
	ds_read_b128 v[114:117], v130 offset:22592
	ds_read_b128 v[118:121], v130 offset:22624
	ds_read_b128 v[122:125], v130 offset:22656
	ds_read_b128 v[132:135], v130 offset:22688
	ds_read_b128 v[136:139], v130 offset:22720
	ds_read_b128 v[140:143], v130 offset:22752
	ds_read_b128 v[146:149], v130 offset:29248
	ds_read_b128 v[150:153], v130 offset:29280
	s_add_i32 s31, s30, 1
	s_cmp_lt_u32 s31, s65
	s_cbranch_scc0 .Lfa_noload_1
	global_load_dwordx4 v[98:101], v[112:113], off
	global_load_dwordx4 v[94:97], v[110:111], off
	s_cmp_lg_u32 s43, 0
	s_cbranch_scc0 .Lfa_noload_1
	global_load_dwordx4 v[90:93], v[108:109], off
.Lfa_noload_1:
	s_waitcnt lgkmcnt(7)
	v_mfma_f32_32x32x16_bf16 v[34:49], v[114:117], v[86:89], 0
	v_add_f32_e32 v105, v105, v50
	v_add_f32_e32 v145, v145, v51
	v_add_f32_e32 v105, v105, v52
	ds_read_b128 v[154:157], v130 offset:29312
	s_waitcnt lgkmcnt(7)
	v_mfma_f32_32x32x16_bf16 v[34:49], v[118:121], v[82:85], v[34:49]
	v_add_f32_e32 v145, v145, v53
	v_add_f32_e32 v105, v105, v54
	v_add_f32_e32 v145, v145, v55
	ds_read_b128 v[158:161], v130 offset:29344
	s_waitcnt lgkmcnt(7)
	v_mfma_f32_32x32x16_bf16 v[34:49], v[122:125], v[78:81], v[34:49]
	v_add_f32_e32 v105, v105, v56
	v_add_f32_e32 v145, v145, v57
	v_add_f32_e32 v105, v105, v58
	ds_read_b128 v[162:165], v130 offset:29376
	s_waitcnt lgkmcnt(7)
	v_mfma_f32_32x32x16_bf16 v[34:49], v[132:135], v[74:77], v[34:49]
	v_add_f32_e32 v145, v145, v59
	v_add_f32_e32 v105, v105, v60
	v_add_f32_e32 v145, v145, v61
	ds_read_b128 v[166:169], v130 offset:29408
	s_waitcnt lgkmcnt(7)
	v_mfma_f32_32x32x16_bf16 v[34:49], v[136:139], v[70:73], v[34:49]
	v_add_f32_e32 v105, v105, v62
	v_add_f32_e32 v145, v145, v63
	s_waitcnt lgkmcnt(6)
	v_mfma_f32_32x32x16_bf16 v[34:49], v[140:143], v[66:69], v[34:49]
	v_add_f32_e32 v105, v105, v64
	v_add_f32_e32 v145, v145, v65
	s_waitcnt lgkmcnt(5)
	v_mfma_f32_32x32x16_bf16 v[50:65], v[146:149], v[86:89], 0
	ds_read_b128 v[114:117], v107 offset:35904
	ds_read_b128 v[118:121], v107 offset:40512
	ds_read_b128 v[122:125], v107 offset:35936
	ds_read_b128 v[132:135], v107 offset:40544
	ds_read_b128 v[136:139], v107 offset:35968
	ds_read_b128 v[140:143], v107 offset:40576
	ds_read_b128 v[146:149], v107 offset:36000
	s_waitcnt lgkmcnt(11)
	v_mfma_f32_32x32x16_bf16 v[50:65], v[150:153], v[82:85], v[50:65]
	ds_read_b128 v[150:153], v107 offset:40608
	v_lshl_add_u64 v[112:113], v[112:113], 0, s[12:13]
	v_lshl_add_u64 v[110:111], v[110:111], 0, v[194:195]
	v_lshl_add_u64 v[108:109], v[108:109], 0, s[10:11]
	v_exp_f32_e32 v34, v34
	v_exp_f32_e32 v35, v35
	s_waitcnt lgkmcnt(11)
	v_mfma_f32_32x32x16_bf16 v[50:65], v[154:157], v[78:81], v[50:65]
	v_exp_f32_e32 v36, v36
	v_exp_f32_e32 v37, v37
	v_exp_f32_e32 v38, v38
	s_waitcnt lgkmcnt(10)
	v_mfma_f32_32x32x16_bf16 v[50:65], v[158:161], v[74:77], v[50:65]
	v_exp_f32_e32 v39, v39
	v_exp_f32_e32 v40, v40
	v_exp_f32_e32 v41, v41
	v_cvt_pk_bf16_f32 v154, v34, v35
	s_waitcnt lgkmcnt(9)
	v_mfma_f32_32x32x16_bf16 v[50:65], v[162:165], v[70:73], v[50:65]
	v_cvt_pk_bf16_f32 v155, v36, v37
	v_cvt_pk_bf16_f32 v156, v38, v39
	v_exp_f32_e32 v42, v42
	v_exp_f32_e32 v43, v43
	s_waitcnt lgkmcnt(8)
	v_mfma_f32_32x32x16_bf16 v[50:65], v[166:169], v[66:69], v[50:65]
	v_cvt_pk_bf16_f32 v157, v40, v41
	v_exp_f32_e32 v44, v44
	v_exp_f32_e32 v45, v45
	v_exp_f32_e32 v46, v46
	s_waitcnt lgkmcnt(7)
	v_mfma_f32_32x32x16_bf16 v[18:33], v[114:117], v[154:157], v[18:33]
	v_exp_f32_e32 v47, v47
	v_exp_f32_e32 v48, v48
	v_exp_f32_e32 v49, v49
	v_cvt_pk_bf16_f32 v158, v42, v43
	s_waitcnt lgkmcnt(6)
	v_mfma_f32_32x32x16_bf16 v[2:17], v[118:121], v[154:157], v[2:17]
	v_cvt_pk_bf16_f32 v159, v44, v45
	v_cvt_pk_bf16_f32 v160, v46, v47
	v_cvt_pk_bf16_f32 v161, v48, v49
	v_add_f32_e32 v105, v105, v34
	v_add_f32_e32 v145, v145, v35
	v_add_f32_e32 v105, v105, v36
	v_exp_f32_e32 v50, v50
	s_waitcnt lgkmcnt(5)
	v_mfma_f32_32x32x16_bf16 v[18:33], v[122:125], v[158:161], v[18:33]
	v_exp_f32_e32 v51, v51
	v_exp_f32_e32 v52, v52
	v_exp_f32_e32 v53, v53
	s_waitcnt lgkmcnt(4)
	v_mfma_f32_32x32x16_bf16 v[2:17], v[132:135], v[158:161], v[2:17]
	v_exp_f32_e32 v54, v54
	v_exp_f32_e32 v55, v55
	v_exp_f32_e32 v56, v56
	v_exp_f32_e32 v57, v57
	v_cvt_pk_bf16_f32 v162, v50, v51
	v_cvt_pk_bf16_f32 v163, v52, v53
	v_cvt_pk_bf16_f32 v164, v54, v55
	v_cvt_pk_bf16_f32 v165, v56, v57
	v_add_f32_e32 v145, v145, v37
	v_add_f32_e32 v105, v105, v38
	s_waitcnt lgkmcnt(3)
	v_mfma_f32_32x32x16_bf16 v[18:33], v[136:139], v[162:165], v[18:33]
	v_exp_f32_e32 v58, v58
	v_exp_f32_e32 v59, v59
	v_exp_f32_e32 v60, v60
	s_waitcnt lgkmcnt(2)
	v_mfma_f32_32x32x16_bf16 v[2:17], v[140:143], v[162:165], v[2:17]
	v_exp_f32_e32 v61, v61
	v_exp_f32_e32 v62, v62
	v_exp_f32_e32 v63, v63
	v_exp_f32_e32 v64, v64
	v_exp_f32_e32 v65, v65
	v_cvt_pk_bf16_f32 v166, v58, v59
	v_cvt_pk_bf16_f32 v167, v60, v61
	v_cvt_pk_bf16_f32 v168, v62, v63
	v_cvt_pk_bf16_f32 v169, v64, v65
	v_add_f32_e32 v145, v145, v39
	v_add_f32_e32 v105, v105, v40
	s_waitcnt lgkmcnt(1)
	v_mfma_f32_32x32x16_bf16 v[18:33], v[146:149], v[166:169], v[18:33]
	v_add_f32_e32 v145, v145, v41
	v_add_f32_e32 v105, v105, v42
	v_add_f32_e32 v145, v145, v43
	v_add_f32_e32 v105, v105, v44
	v_add_f32_e32 v145, v145, v45
	s_waitcnt lgkmcnt(0)
	v_mfma_f32_32x32x16_bf16 v[2:17], v[150:153], v[166:169], v[2:17]
	v_add_f32_e32 v105, v105, v46
	v_add_f32_e32 v145, v145, v47
	v_add_f32_e32 v105, v105, v48
	v_add_f32_e32 v145, v145, v49
	s_cmp_lt_u32 s31, s65
	s_cbranch_scc0 .Lfa_nowrite_1
	s_waitcnt vmcnt(0)
	ds_write_b128 v106, v[98:101] offset:64
	ds_write_b128 v128, v[94:97] offset:64
	s_cmp_lg_u32 s43, 0
	s_cbranch_scc0 .Lfa_nowrite_1
	ds_write_b128 v129, v[90:93] offset:13376
